# baseline (speedup 1.0000x reference)
.Lk2_l2_done:
	s_or_b64 s[94:95], s[36:37], s[40:41]
	s_mov_b64 s[52:53], 0
	s_mov_b64 s[50:51], s[36:37]

.Lk2_nohard:
	s_mov_b32 s52, s98
	s_mov_b32 s53, s99
	v_and_b32_e32 v69, 63, v1
	v_lshlrev_b32_e32 v69, 4, v69
	v_add_u32_e32 v70, 0x1000, v69
	s_and_b32 s54, s52, 0xffff
	s_lshr_b32 s55, s52, 16
	s_and_b32 s56, s53, 0xffff
	s_lshr_b32 s57, s53, 16
	s_cmp_gt_u32 s55, 1
	s_cselect_b32 s58, 1, 0
	s_cmp_lt_u32 s54, 0x64
	s_cselect_b32 s59, 1, 0
	s_and_b32 s58, s58, s59
	s_cmp_gt_u32 s57, 1
	s_cselect_b32 s60, 1, 0
	s_cmp_lt_u32 s56, 0x64
	s_cselect_b32 s61, 1, 0
	s_and_b32 s60, s60, s61
	s_or_b32 s61, s58, s60
	s_lshl_b32 s62, s25, 3
	s_lshl_b32 s63, s27, 1
	s_add_u32 s62, s62, s63
	s_add_u32 s62, s62, s26
	s_lshl_b32 s62, s62, 13
	s_add_u32 s64, s6, s62
	s_addc_u32 s65, s7, 0
	s_add_u32 s66, s64, 0x2000
	s_addc_u32 s67, s65, 0
	s_mov_b32 s92, 0
	s_cmp_eq_u64 s[94:95], 0
	s_cbranch_scc0 .Lk2_noearly
	s_cmp_lt_u32 s54, 0x64
	s_cbranch_scc0 .Lk2_ea_skip
	global_load_dwordx4 v[32:35], v69, s[64:65] offset:0 nt
	global_load_dwordx4 v[36:39], v69, s[64:65] offset:1024 nt
	global_load_dwordx4 v[40:43], v69, s[64:65] offset:2048 nt
	global_load_dwordx4 v[44:47], v69, s[64:65] offset:3072 nt
	global_load_dwordx4 v[48:51], v70, s[64:65] offset:0 nt
	global_load_dwordx4 v[52:55], v70, s[64:65] offset:1024 nt
	global_load_dwordx4 v[56:59], v70, s[64:65] offset:2048 nt
	global_load_dwordx4 v[60:63], v70, s[64:65] offset:3072 nt
	s_or_b32 s92, s92, 1
.Lk2_ea_skip:
	s_cmp_lt_u32 s56, 0x64
	s_cbranch_scc0 .Lk2_noearly
	global_load_dwordx4 v[72:75], v69, s[66:67] offset:0 nt
	global_load_dwordx4 v[76:79], v69, s[66:67] offset:1024 nt
	global_load_dwordx4 v[80:83], v69, s[66:67] offset:2048 nt
	global_load_dwordx4 v[84:87], v69, s[66:67] offset:3072 nt
	global_load_dwordx4 v[88:91], v70, s[66:67] offset:0 nt
	global_load_dwordx4 v[92:95], v70, s[66:67] offset:1024 nt
	global_load_dwordx4 v[96:99], v70, s[66:67] offset:2048 nt
	global_load_dwordx4 v[100:103], v70, s[66:67] offset:3072 nt
	s_or_b32 s92, s92, 2
.Lk2_noearly:
	s_waitcnt lgkmcnt(0)
	s_barrier
	ds_read_b128 v[108:111], v105
	ds_read_b32 v112, v105 offset:24
	v_lshrrev_b32_e32 v29, 5, v1
	v_and_b32_e32 v31, 31, v1
	v_lshl_add_u32 v29, s25, 3, v29
	v_lshlrev_b32_e32 v29, 3, v29
	v_lshlrev_b32_e32 v31, 3, v31
	s_waitcnt lgkmcnt(0)
	v_readfirstlane_b32 s31, v110
	v_readfirstlane_b32 s74, v108
	s_cmp_lg_u32 s31, 0
	s_cbranch_scc1 .Lk2_fallback
	s_cmp_lg_u32 s74, 0
	s_cbranch_scc1 .Lk2_hard
	v_readfirstlane_b32 s31, v112
	s_cmp_lg_u32 s31, 0
	s_cbranch_scc0 .Lk2_issue
.Lk2_rank:
	ds_read_b64 v[116:117], v29 offset:0
	v_mov_b32_e32 v118, 0
	v_mov_b32_e32 v119, 0
	ds_read_b64 v[108:109], v31 offset:0
	ds_read_b64 v[110:111], v31 offset:256
	ds_read_b64 v[112:113], v31 offset:512
	ds_read_b64 v[114:115], v31 offset:768
	s_waitcnt lgkmcnt(0)
	v_add_f64 v[120:121], v[108:109], -v[116:117]
	v_cmp_lt_f64_e32 vcc, s[32:33], v[120:121]
	v_cmp_ge_f64_e64 s[48:49], s[32:33], |v[120:121]|
	s_nop 0
	v_addc_co_u32_e32 v118, vcc, 0, v118, vcc
	v_addc_co_u32_e64 v119, s[50:51], 0, v119, s[48:49]
	v_add_f64 v[120:121], v[110:111], -v[116:117]
	v_cmp_lt_f64_e32 vcc, s[32:33], v[120:121]
	v_cmp_ge_f64_e64 s[48:49], s[32:33], |v[120:121]|
	s_nop 0
	v_addc_co_u32_e32 v118, vcc, 0, v118, vcc
	v_addc_co_u32_e64 v119, s[50:51], 0, v119, s[48:49]
	v_add_f64 v[120:121], v[112:113], -v[116:117]
	v_cmp_lt_f64_e32 vcc, s[32:33], v[120:121]
	v_cmp_ge_f64_e64 s[48:49], s[32:33], |v[120:121]|
	s_nop 0
	v_addc_co_u32_e32 v118, vcc, 0, v118, vcc
	v_addc_co_u32_e64 v119, s[50:51], 0, v119, s[48:49]
	v_add_f64 v[120:121], v[114:115], -v[116:117]
	v_cmp_lt_f64_e32 vcc, s[32:33], v[120:121]
	v_cmp_ge_f64_e64 s[48:49], s[32:33], |v[120:121]|
	s_nop 0
	v_addc_co_u32_e32 v118, vcc, 0, v118, vcc
	v_addc_co_u32_e64 v119, s[50:51], 0, v119, s[48:49]
	ds_read_b64 v[108:109], v31 offset:1024
	ds_read_b64 v[110:111], v31 offset:1280
	ds_read_b64 v[112:113], v31 offset:1536
	ds_read_b64 v[114:115], v31 offset:1792
	s_waitcnt lgkmcnt(0)
	v_add_f64 v[120:121], v[108:109], -v[116:117]
	v_cmp_lt_f64_e32 vcc, s[32:33], v[120:121]
	v_cmp_ge_f64_e64 s[48:49], s[32:33], |v[120:121]|
	s_nop 0
	v_addc_co_u32_e32 v118, vcc, 0, v118, vcc
	v_addc_co_u32_e64 v119, s[50:51], 0, v119, s[48:49]
	v_add_f64 v[120:121], v[110:111], -v[116:117]
	v_cmp_lt_f64_e32 vcc, s[32:33], v[120:121]
	v_cmp_ge_f64_e64 s[48:49], s[32:33], |v[120:121]|
	s_nop 0
	v_addc_co_u32_e32 v118, vcc, 0, v118, vcc
	v_addc_co_u32_e64 v119, s[50:51], 0, v119, s[48:49]
	v_add_f64 v[120:121], v[112:113], -v[116:117]
	v_cmp_lt_f64_e32 vcc, s[32:33], v[120:121]
	v_cmp_ge_f64_e64 s[48:49], s[32:33], |v[120:121]|
	s_nop 0
	v_addc_co_u32_e32 v118, vcc, 0, v118, vcc
	v_addc_co_u32_e64 v119, s[50:51], 0, v119, s[48:49]
	v_add_f64 v[120:121], v[114:115], -v[116:117]
	v_cmp_lt_f64_e32 vcc, s[32:33], v[120:121]
	v_cmp_ge_f64_e64 s[48:49], s[32:33], |v[120:121]|
	s_nop 0
	v_addc_co_u32_e32 v118, vcc, 0, v118, vcc
	v_addc_co_u32_e64 v119, s[50:51], 0, v119, s[48:49]
	ds_read_b64 v[108:109], v31 offset:2048
	ds_read_b64 v[110:111], v31 offset:2304
	ds_read_b64 v[112:113], v31 offset:2560
	ds_read_b64 v[114:115], v31 offset:2816
	s_waitcnt lgkmcnt(0)
	v_add_f64 v[120:121], v[108:109], -v[116:117]
	v_cmp_lt_f64_e32 vcc, s[32:33], v[120:121]
	v_cmp_ge_f64_e64 s[48:49], s[32:33], |v[120:121]|
	s_nop 0
	v_addc_co_u32_e32 v118, vcc, 0, v118, vcc
	v_addc_co_u32_e64 v119, s[50:51], 0, v119, s[48:49]
	v_add_f64 v[120:121], v[110:111], -v[116:117]
	v_cmp_lt_f64_e32 vcc, s[32:33], v[120:121]
	v_cmp_ge_f64_e64 s[48:49], s[32:33], |v[120:121]|
	s_nop 0
	v_addc_co_u32_e32 v118, vcc, 0, v118, vcc
	v_addc_co_u32_e64 v119, s[50:51], 0, v119, s[48:49]
	v_add_f64 v[120:121], v[112:113], -v[116:117]
	v_cmp_lt_f64_e32 vcc, s[32:33], v[120:121]
	v_cmp_ge_f64_e64 s[48:49], s[32:33], |v[120:121]|
	s_nop 0
	v_addc_co_u32_e32 v118, vcc, 0, v118, vcc
	v_addc_co_u32_e64 v119, s[50:51], 0, v119, s[48:49]
	v_add_f64 v[120:121], v[114:115], -v[116:117]
	v_cmp_lt_f64_e32 vcc, s[32:33], v[120:121]
	v_cmp_ge_f64_e64 s[48:49], s[32:33], |v[120:121]|
	s_nop 0
	v_addc_co_u32_e32 v118, vcc, 0, v118, vcc
	v_addc_co_u32_e64 v119, s[50:51], 0, v119, s[48:49]
	ds_read_b64 v[108:109], v31 offset:3072
	ds_read_b64 v[110:111], v31 offset:3328
	ds_read_b64 v[112:113], v31 offset:3584
	ds_read_b64 v[114:115], v31 offset:3840
	s_waitcnt lgkmcnt(0)
	v_add_f64 v[120:121], v[108:109], -v[116:117]
	v_cmp_lt_f64_e32 vcc, s[32:33], v[120:121]
	v_cmp_ge_f64_e64 s[48:49], s[32:33], |v[120:121]|
	s_nop 0
	v_addc_co_u32_e32 v118, vcc, 0, v118, vcc
	v_addc_co_u32_e64 v119, s[50:51], 0, v119, s[48:49]
	v_add_f64 v[120:121], v[110:111], -v[116:117]
	v_cmp_lt_f64_e32 vcc, s[32:33], v[120:121]
	v_cmp_ge_f64_e64 s[48:49], s[32:33], |v[120:121]|
	s_nop 0
	v_addc_co_u32_e32 v118, vcc, 0, v118, vcc
	v_addc_co_u32_e64 v119, s[50:51], 0, v119, s[48:49]
	v_add_f64 v[120:121], v[112:113], -v[116:117]
	v_cmp_lt_f64_e32 vcc, s[32:33], v[120:121]
	v_cmp_ge_f64_e64 s[48:49], s[32:33], |v[120:121]|
	s_nop 0
	v_addc_co_u32_e32 v118, vcc, 0, v118, vcc
	v_addc_co_u32_e64 v119, s[50:51], 0, v119, s[48:49]
	v_add_f64 v[120:121], v[114:115], -v[116:117]
	v_cmp_lt_f64_e32 vcc, s[32:33], v[120:121]
	v_cmp_ge_f64_e64 s[48:49], s[32:33], |v[120:121]|
	s_nop 0
	v_addc_co_u32_e32 v118, vcc, 0, v118, vcc
	v_addc_co_u32_e64 v119, s[50:51], 0, v119, s[48:49]
	v_lshl_or_b32 v122, v119, 16, v118
	s_nop 1
	v_add_u32_dpp v122, v122, v122 quad_perm:[1,0,3,2] row_mask:0xf bank_mask:0xf
	s_nop 1
	v_add_u32_dpp v122, v122, v122 quad_perm:[2,3,0,1] row_mask:0xf bank_mask:0xf
	s_nop 1
	v_add_u32_dpp v122, v122, v122 row_half_mirror row_mask:0xf bank_mask:0xf
	s_nop 1
	v_add_u32_dpp v122, v122, v122 row_mirror row_mask:0xf bank_mask:0xf
	s_nop 1
	v_add_u32_dpp v122, v122, v122 row_bcast:15 row_mask:0xa bank_mask:0xf
	s_nop 1
	v_readlane_b32 s52, v122, 31
	v_readlane_b32 s53, v122, 63
.Lk2_ranked:
	s_and_b32 s54, s52, 0xffff
	s_lshr_b32 s55, s52, 16
	s_and_b32 s56, s53, 0xffff
	s_lshr_b32 s57, s53, 16
	s_cmp_gt_u32 s55, 1
	s_cselect_b32 s58, 1, 0
	s_cmp_lt_u32 s54, 0x64
	s_cselect_b32 s59, 1, 0
	s_and_b32 s58, s58, s59
	s_cmp_gt_u32 s57, 1
	s_cselect_b32 s60, 1, 0
	s_cmp_lt_u32 s56, 0x64
	s_cselect_b32 s61, 1, 0
	s_and_b32 s60, s60, s61
	s_or_b32 s61, s58, s60
.Lk2_issue:
	s_mov_b32 s93, 0
	s_cmp_lt_u32 s54, 0x64
	s_cbranch_scc0 .Lk2_ga_skip
	s_bitcmp1_b32 s92, 0
	s_cbranch_scc1 .Lk2_ga_skip
	global_load_dwordx4 v[32:35], v69, s[64:65] offset:0 nt
	global_load_dwordx4 v[36:39], v69, s[64:65] offset:1024 nt
	global_load_dwordx4 v[40:43], v69, s[64:65] offset:2048 nt
	global_load_dwordx4 v[44:47], v69, s[64:65] offset:3072 nt
	global_load_dwordx4 v[48:51], v70, s[64:65] offset:0 nt
	global_load_dwordx4 v[52:55], v70, s[64:65] offset:1024 nt
	global_load_dwordx4 v[56:59], v70, s[64:65] offset:2048 nt
	global_load_dwordx4 v[60:63], v70, s[64:65] offset:3072 nt
	s_mov_b32 s93, 1
.Lk2_ga_skip:
	s_cmp_lt_u32 s56, 0x64
	s_cbranch_scc0 .Lk2_gb_skip
	s_bitcmp1_b32 s92, 1
	s_cbranch_scc1 .Lk2_gb_skip
	global_load_dwordx4 v[72:75], v69, s[66:67] offset:0 nt
	global_load_dwordx4 v[76:79], v69, s[66:67] offset:1024 nt
	global_load_dwordx4 v[80:83], v69, s[66:67] offset:2048 nt
	global_load_dwordx4 v[84:87], v69, s[66:67] offset:3072 nt
	global_load_dwordx4 v[88:91], v70, s[66:67] offset:0 nt
	global_load_dwordx4 v[92:95], v70, s[66:67] offset:1024 nt
	global_load_dwordx4 v[96:99], v70, s[66:67] offset:2048 nt
	global_load_dwordx4 v[100:103], v70, s[66:67] offset:3072 nt
	s_mov_b32 s93, 1
.Lk2_gb_skip:
	s_cmp_eq_u32 s92, 0
	s_cbranch_scc1 .Lk2_nofix
	s_cmp_eq_u32 s93, 0
	s_cbranch_scc1 .Lk2_nofix
	s_waitcnt vmcnt(0)

.Lk2_hard:
	s_waitcnt vmcnt(0)
	s_mov_b32 s92, 0
	s_mov_b32 s75, 0
	s_mov_b32 s83, 0
